# P4 pass 2: importance LDS adds no longer drain the next block DMA; P5 tile combine: MIXACC chunk loads issued up front with counted waits
# speedup vs baseline: 1.0008x; 1.0008x over previous
; template <int PASS, bool FULL = false> __device__ __forceinline__ bf16x8 cmp_sm(const f32x4 s0, const f32x4 s1, float& l, float mbi  , LAS float* improw, int kg, int i, int g4, int tq, int j, float mb) {
;     float p[8];
; #pragma unroll
;     for (int r = 0; r < 8; ++r) { const int key = 64 * j + 32 * kg + 8 * g4 + r; const float sv = r < 4 ? s0[r & 3] : s1[r & 3];
; template <int PASS> __device__ __forceinline__ void cmp_compute2(LAS const unsigned char* kb, const QF& q0, const QF& q1, f32x4 (&O0)[8], f32x4 (&O1)[8], float& l0, float& l1, float inv0, float inv1, LAS float* imp0, LAS float* imp1, int i, int g4, int tq0, int tq1, int j, float mb, bool full) {
;     LAS const unsigned char* vb = kb + 16384;
;     bf16x8 ka0[4], ka1[4], kb0[4], kb1[4]; f32x4 s0, s1, t0, t1, u0, u1, v0, v1;
;     ta_ldk(kb, 0, i, g4, ka0, ka1); ta_ldk(kb, 1, i, g4, kb0, kb1); TA_SB;
;     ta_qk(ka0, ka1, q0, s0, s1); ta_qk(kb0, kb1, q0, t0, t1); TA_SB;
;     ta_qk(ka0, ka1, q1, u0, u1); ta_qk(kb0, kb1, q1, v0, v1); TA_SB;
;     if (PASS == 1) {
;         if (full) { (void)cmp_sm<1, true>(s0, s1, l0, inv0, imp0, 0, i, g4, tq0, j, mb); (void)cmp_sm<1, true>(t0, t1, l0, inv0, imp0, 1, i, g4, tq0, j, mb);
;                     (void)cmp_sm<1, true>(u0, u1, l1, inv1, imp1, 0, i, g4, tq1, j, mb); (void)cmp_sm<1, true>(v0, v1, l1, inv1, imp1, 1, i, g4, tq1, j, mb); }
;         else { (void)cmp_sm<1>(s0, s1, l0, inv0, imp0, 0, i, g4, tq0, j, mb); (void)cmp_sm<1>(t0, t1, l0, inv0, imp0, 1, i, g4, tq0, j, mb);
;                (void)cmp_sm<1>(u0, u1, l1, inv1, imp1, 0, i, g4, tq1, j, mb); (void)cmp_sm<1>(v0, v1, l1, inv1, imp1, 1, i, g4, tq1, j, mb); }
;         TA_SB; }
;     else { bf16x8 va[8], vc[8], pa0, pb0, pa1, pb1;
;         ta_ldv(vb, 0, i, g4, va); TA_SB;
;         if (full) { pa0 = cmp_sm<2, true>(s0, s1, l0, inv0, imp0, 0, i, g4, tq0, j, mb); pb0 = cmp_sm<2, true>(t0, t1, l0, inv0, imp0, 1, i, g4, tq0, j, mb);
;                     pa1 = cmp_sm<2, true>(u0, u1, l1, inv1, imp1, 0, i, g4, tq1, j, mb); pb1 = cmp_sm<2, true>(v0, v1, l1, inv1, imp1, 1, i, g4, tq1, j, mb); }
;         else { pa0 = cmp_sm<2>(s0, s1, l0, inv0, imp0, 0, i, g4, tq0, j, mb); pb0 = cmp_sm<2>(t0, t1, l0, inv0, imp0, 1, i, g4, tq0, j, mb);
;                pa1 = cmp_sm<2>(u0, u1, l1, inv1, imp1, 0, i, g4, tq1, j, mb); pb1 = cmp_sm<2>(v0, v1, l1, inv1, imp1, 1, i, g4, tq1, j, mb); }
.LBB0_564:
	s_add_i32 s0, s11, 0xffff8000
	s_and_b32 s0, s0, 0x8000
	s_add_i32 s0, s0, 0
	v_add_u32_e32 v122, s0, v214
	v_add_u32_e32 v134, v122, v215
	v_add_u32_e32 v142, v122, v216
	v_add_u32_e32 v143, v122, v217
	v_add_u32_e32 v144, v122, v218
	ds_read_b128 v[98:101], v134
	ds_read_b128 v[102:105], v134 offset:1024
	ds_read_b128 v[106:109], v142
	ds_read_b128 v[110:113], v142 offset:1024
	ds_read_b128 v[114:117], v143
	ds_read_b128 v[118:121], v143 offset:1024
	ds_read_b128 v[122:125], v144
	ds_read_b128 v[126:129], v144 offset:1024
	ds_read_b128 v[130:133], v134 offset:8192
	ds_read_b128 v[134:137], v134 offset:9216
	ds_read_b128 v[138:141], v142 offset:8192
	ds_read_b128 v[150:153], v142 offset:9216
	ds_read_b128 v[162:165], v143 offset:8192
	ds_read_b128 v[166:169], v143 offset:9216
	ds_read_b128 v[236:239], v144 offset:8192
	ds_read_b128 v[240:243], v144 offset:9216
	s_cmp_gt_i32 s10, s5
	s_waitcnt lgkmcnt(8)
	v_mfma_f32_16x16x32_bf16 v[142:145], v[98:101], v[2:5], 0
	v_mfma_f32_16x16x32_bf16 v[146:149], v[102:105], v[2:5], 0
	v_mfma_f32_16x16x32_bf16 v[142:145], v[106:109], v[6:9], v[142:145]
	v_mfma_f32_16x16x32_bf16 v[146:149], v[110:113], v[6:9], v[146:149]
	v_mfma_f32_16x16x32_bf16 v[142:145], v[114:117], v[10:13], v[142:145]
	v_mfma_f32_16x16x32_bf16 v[146:149], v[118:121], v[10:13], v[146:149]
	v_mfma_f32_16x16x32_bf16 v[244:247], v[122:125], v[14:17], v[142:145]
	v_mfma_f32_16x16x32_bf16 v[248:251], v[126:129], v[14:17], v[146:149]
	s_waitcnt lgkmcnt(0)
	v_mfma_f32_16x16x32_bf16 v[142:145], v[130:133], v[2:5], 0
	v_mfma_f32_16x16x32_bf16 v[146:149], v[134:137], v[2:5], 0
	v_mfma_f32_16x16x32_bf16 v[142:145], v[138:141], v[6:9], v[142:145]
	v_mfma_f32_16x16x32_bf16 v[146:149], v[150:153], v[6:9], v[146:149]
	v_mfma_f32_16x16x32_bf16 v[142:145], v[162:165], v[10:13], v[142:145]
	v_mfma_f32_16x16x32_bf16 v[146:149], v[166:169], v[10:13], v[146:149]
	v_mfma_f32_16x16x32_bf16 v[158:161], v[236:239], v[14:17], v[142:145]
	v_mfma_f32_16x16x32_bf16 v[154:157], v[240:243], v[14:17], v[146:149]
	v_mfma_f32_16x16x32_bf16 v[98:101], v[98:101], v[18:21], 0
	v_mfma_f32_16x16x32_bf16 v[102:105], v[102:105], v[18:21], 0
	v_mfma_f32_16x16x32_bf16 v[98:101], v[106:109], v[22:25], v[98:101]
	v_mfma_f32_16x16x32_bf16 v[102:105], v[110:113], v[22:25], v[102:105]
	v_mfma_f32_16x16x32_bf16 v[98:101], v[114:117], v[26:29], v[98:101]
	v_mfma_f32_16x16x32_bf16 v[102:105], v[118:121], v[26:29], v[102:105]
	v_mfma_f32_16x16x32_bf16 v[146:149], v[122:125], v[30:33], v[98:101]
	v_mfma_f32_16x16x32_bf16 v[142:145], v[126:129], v[30:33], v[102:105]
	v_mfma_f32_16x16x32_bf16 v[98:101], v[130:133], v[18:21], 0
	v_mfma_f32_16x16x32_bf16 v[102:105], v[134:137], v[18:21], 0
	v_mfma_f32_16x16x32_bf16 v[98:101], v[138:141], v[22:25], v[98:101]
	v_mfma_f32_16x16x32_bf16 v[102:105], v[150:153], v[22:25], v[102:105]
	v_mfma_f32_16x16x32_bf16 v[98:101], v[162:165], v[26:29], v[98:101]
	v_mfma_f32_16x16x32_bf16 v[102:105], v[166:169], v[26:29], v[102:105]
	v_mfma_f32_16x16x32_bf16 v[138:141], v[236:239], v[30:33], v[98:101]
	v_mfma_f32_16x16x32_bf16 v[134:137], v[240:243], v[30:33], v[102:105]
	v_add_u32_e32 v236, s0, v220
	v_add_u32_e32 v126, v236, v221
	s_nop 2
	ds_read_b128 v[98:101], v126 offset:16384
	ds_read_b128 v[102:105], v126 offset:18432
	ds_read_b128 v[106:109], v126 offset:20480
	ds_read_b128 v[110:113], v126 offset:22528
	ds_read_b128 v[114:117], v126 offset:24576
	ds_read_b128 v[118:121], v126 offset:26624
	ds_read_b128 v[122:125], v126 offset:28672
	ds_read_b128 v[126:129], v126 offset:30720
	s_mov_b64 s[0:1], -1
	v_fma_f32 v244, v244, s55, -v199
	v_fma_f32 v243, v245, s55, -v199
	v_fma_f32 v242, v246, s55, -v199
	v_fma_f32 v241, v247, s55, -v199
	v_fma_f32 v240, v248, s55, -v199
	v_fma_f32 v239, v249, s55, -v199
	v_fma_f32 v238, v250, s55, -v199
	v_fma_f32 v237, v251, s55, -v199
	s_cbranch_scc1 .LBB0_574
	v_exp_f32_e32 v132, v240
	v_exp_f32_e32 v151, v239
	v_exp_f32_e32 v130, v244
	v_exp_f32_e32 v153, v243
	v_exp_f32_e32 v133, v238
	v_exp_f32_e32 v131, v242
	v_exp_f32_e32 v152, v241
	v_exp_f32_e32 v150, v237
	v_add_f32_e32 v163, v132, v151
	v_add_f32_e32 v162, v130, v153
	v_add_f32_e32 v163, v133, v163
	v_add_f32_e32 v162, v131, v162
	v_fma_f32 v163, 2.0, v163, v152
	v_fma_f32 v162, 2.0, v162, v152
	v_add_f32_e32 v164, v150, v163
	v_add_f32_dpp v166, v150, v150 quad_perm:[1,0,3,2] row_mask:0xf bank_mask:0xf bound_ctrl:1
	v_add_f32_dpp v162, v162, v162 quad_perm:[1,0,3,2] row_mask:0xf bank_mask:0xf bound_ctrl:1
	v_add_f32_dpp v164, v164, v164 quad_perm:[1,0,3,2] row_mask:0xf bank_mask:0xf bound_ctrl:1
	v_mov_b32_dpp v167, v166 quad_perm:[2,3,0,1] row_mask:0xf bank_mask:0xf bound_ctrl:1
	v_mov_b32_dpp v163, v162 quad_perm:[2,3,0,1] row_mask:0xf bank_mask:0xf bound_ctrl:1
	v_mov_b32_dpp v165, v164 quad_perm:[2,3,0,1] row_mask:0xf bank_mask:0xf bound_ctrl:1
	s_and_saveexec_b64 s[0:1], s[8:9]
	s_cbranch_execz .LBB0_567
	v_add_f32_e32 v162, v162, v163
	v_add_f32_e32 v163, v164, v165
	v_add_f32_e32 v164, v166, v167
	s_nop 0
	ds_add_f32 v203, v162
	ds_add_f32 v203, v163 offset:4
	ds_add_f32 v203, v164 offset:8
; #define LAS __attribute__((address_space(3)))
; template <int CTRL> __device__ __forceinline__ float dppf(float v) { return __builtin_bit_cast(float, __builtin_amdgcn_update_dpp(0, __builtin_bit_cast(int, v), CTRL, 0xF, 0xF, true)); }
; template <int PASS, bool FULL = false> __device__ __forceinline__ bf16x8 cmp_sm(const f32x4 s0, const f32x4 s1, float& l, float mbi  , LAS float* improw, int kg, int i, int g4, int tq, int j, float mb) {
;     float p[8];
; #pragma unroll
;     for (int r = 0; r < 8; ++r) { const int key = 64 * j + 32 * kg + 8 * g4 + r; const float sv = r < 4 ? s0[r & 3] : s1[r & 3];
;         const float e = __builtin_amdgcn_exp2f(sv * C2_ - (PASS == 1 ? mb : mbi));
;         p[r] = (FULL || 16 * key + 31 <= tq) ? e : 0.f; }
;     if (PASS == 1) { l += ((p[0] + p[1]) + (p[2] + p[3])) + ((p[4] + p[5]) + (p[6] + p[7])); return (bf16x8){0, 0, 0, 0, 0, 0, 0, 0}; }
;     float ia = 2.0f * (p[0] + p[1] + p[2]) + p[3], ib = p[3] + 2.0f * (p[4] + p[5] + p[6]) + p[7], ic = p[7];
;     ia += dppf<0xB1>(ia); ia += dppf<0x4E>(ia); ib += dppf<0xB1>(ib); ib += dppf<0x4E>(ib); ic += dppf<0xB1>(ic); ic += dppf<0x4E>(ic);
;     if ((i & 3) == 0) { LAS float* ip = improw + 16 * j + 8 * kg + 2 * g4;
;         __hip_atomic_fetch_add(ip, ia, __ATOMIC_RELAXED, __HIP_MEMORY_SCOPE_WORKGROUP); __hip_atomic_fetch_add(ip + 1, ib, __ATOMIC_RELAXED, __HIP_MEMORY_SCOPE_WORKGROUP); __hip_atomic_fetch_add(ip + 2, ic, __ATOMIC_RELAXED, __HIP_MEMORY_SCOPE_WORKGROUP); }
;     return pack8(p[0], p[1], p[2], p[3], p[4], p[5], p[6], p[7]);
; template <int PASS> __device__ __forceinline__ void cmp_compute2(LAS const unsigned char* kb, const QF& q0, const QF& q1, f32x4 (&O0)[8], f32x4 (&O1)[8], float& l0, float& l1, float inv0, float inv1, LAS float* imp0, LAS float* imp1, int i, int g4, int tq0, int tq1, int j, float mb, bool full) {
;     ...
;         if (full) { pa0 = cmp_sm<2, true>(s0, s1, l0, inv0, imp0, 0, i, g4, tq0, j, mb); pb0 = cmp_sm<2, true>(t0, t1, l0, inv0, imp0, 1, i, g4, tq0, j, mb);
;                     pa1 = cmp_sm<2, true>(u0, u1, l1, inv1, imp1, 0, i, g4, tq1, j, mb); pb1 = cmp_sm<2, true>(v0, v1, l1, inv1, imp1, 1, i, g4, tq1, j, mb); }
.LBB0_567:
	s_or_b64 exec, exec, s[0:1]
	v_cvt_pk_bf16_f32 v130, v130, v153
	v_fma_f32 v153, v161, s55, -v199
	v_exp_f32_e32 v162, v153
	v_fma_f32 v153, v154, s55, -v199
	v_fma_f32 v163, v155, s55, -v199
	v_cvt_pk_bf16_f32 v131, v131, v152
	v_cvt_pk_bf16_f32 v132, v132, v151
	v_cvt_pk_bf16_f32 v133, v133, v150
	v_fma_f32 v150, v158, s55, -v199
	v_fma_f32 v151, v159, s55, -v199
	v_exp_f32_e32 v153, v153
	v_exp_f32_e32 v164, v163
	v_fma_f32 v163, v156, s55, -v199
	v_exp_f32_e32 v150, v150
	v_exp_f32_e32 v152, v151
	v_fma_f32 v151, v160, s55, -v199
	v_exp_f32_e32 v163, v163
	v_exp_f32_e32 v151, v151
	v_fma_f32 v165, v157, s55, -v199
	v_exp_f32_e32 v165, v165
	v_add_f32_e32 v167, v153, v164
	v_add_f32_e32 v166, v150, v152
	v_add_f32_e32 v167, v163, v167
	v_add_f32_e32 v166, v151, v166
	v_fma_f32 v167, 2.0, v167, v162
	v_fma_f32 v166, 2.0, v166, v162
	v_add_f32_e32 v168, v165, v167
	v_add_f32_dpp v245, v165, v165 quad_perm:[1,0,3,2] row_mask:0xf bank_mask:0xf bound_ctrl:1
	v_add_f32_dpp v166, v166, v166 quad_perm:[1,0,3,2] row_mask:0xf bank_mask:0xf bound_ctrl:1
	v_add_f32_dpp v168, v168, v168 quad_perm:[1,0,3,2] row_mask:0xf bank_mask:0xf bound_ctrl:1
	v_mov_b32_dpp v246, v245 quad_perm:[2,3,0,1] row_mask:0xf bank_mask:0xf bound_ctrl:1
	v_mov_b32_dpp v167, v166 quad_perm:[2,3,0,1] row_mask:0xf bank_mask:0xf bound_ctrl:1
	v_mov_b32_dpp v169, v168 quad_perm:[2,3,0,1] row_mask:0xf bank_mask:0xf bound_ctrl:1
	s_and_saveexec_b64 s[0:1], s[8:9]
	s_cbranch_execz .LBB0_569
	v_add_f32_e32 v166, v166, v167
	v_add_f32_e32 v167, v168, v169
	v_add_f32_e32 v168, v245, v246
	s_nop 0
	ds_add_f32 v203, v166 offset:32
	ds_add_f32 v203, v167 offset:36
	ds_add_f32 v203, v168 offset:40
.LBB0_569:
	s_or_b64 exec, exec, s[0:1]
	v_cvt_pk_bf16_f32 v150, v150, v152
	v_cvt_pk_bf16_f32 v151, v151, v162
	v_cvt_pk_bf16_f32 v152, v153, v164
	v_cvt_pk_bf16_f32 v153, v163, v165
	v_fma_f32 v165, v149, s55, -v201
	v_exp_f32_e32 v166, v165
	v_fma_f32 v165, v142, s55, -v201
	v_fma_f32 v167, v143, s55, -v201
	v_fma_f32 v162, v146, s55, -v201
	v_fma_f32 v163, v147, s55, -v201
	v_exp_f32_e32 v165, v165
	v_exp_f32_e32 v168, v167
	v_fma_f32 v167, v144, s55, -v201
	v_exp_f32_e32 v162, v162
	v_exp_f32_e32 v164, v163
	v_fma_f32 v163, v148, s55, -v201
	v_exp_f32_e32 v167, v167
	v_exp_f32_e32 v163, v163
	v_fma_f32 v169, v145, s55, -v201
	v_exp_f32_e32 v169, v169
	v_add_f32_e32 v245, v165, v168
	v_add_f32_e32 v225, v162, v164
	v_add_f32_e32 v245, v167, v245
	v_add_f32_e32 v225, v163, v225
	v_fma_f32 v245, 2.0, v245, v166
	v_fma_f32 v225, 2.0, v225, v166
	v_add_f32_e32 v247, v169, v245
	v_add_f32_dpp v249, v169, v169 quad_perm:[1,0,3,2] row_mask:0xf bank_mask:0xf bound_ctrl:1
	v_add_f32_dpp v245, v225, v225 quad_perm:[1,0,3,2] row_mask:0xf bank_mask:0xf bound_ctrl:1
	v_add_f32_dpp v247, v247, v247 quad_perm:[1,0,3,2] row_mask:0xf bank_mask:0xf bound_ctrl:1
	v_mov_b32_dpp v250, v249 quad_perm:[2,3,0,1] row_mask:0xf bank_mask:0xf bound_ctrl:1
	v_mov_b32_dpp v246, v245 quad_perm:[2,3,0,1] row_mask:0xf bank_mask:0xf bound_ctrl:1
	v_mov_b32_dpp v248, v247 quad_perm:[2,3,0,1] row_mask:0xf bank_mask:0xf bound_ctrl:1
	s_and_saveexec_b64 s[0:1], s[8:9]
	s_cbranch_execz .LBB0_571
	v_add_f32_e32 v225, v245, v246
	v_add_f32_e32 v245, v247, v248
	v_add_f32_e32 v246, v249, v250
	s_nop 0
	ds_add_f32 v203, v225 offset:4112
	ds_add_f32 v203, v245 offset:4116
	ds_add_f32 v203, v246 offset:4120
.LBB0_571:
	s_or_b64 exec, exec, s[0:1]
	v_cvt_pk_bf16_f32 v162, v162, v164
	v_cvt_pk_bf16_f32 v163, v163, v166
	v_cvt_pk_bf16_f32 v164, v165, v168
	v_cvt_pk_bf16_f32 v165, v167, v169
	v_fma_f32 v169, v141, s55, -v201
	v_exp_f32_e32 v245, v169
	v_fma_f32 v169, v134, s55, -v201
	v_fma_f32 v225, v135, s55, -v201
	v_fma_f32 v166, v138, s55, -v201
	v_fma_f32 v167, v139, s55, -v201
	v_exp_f32_e32 v169, v169
	v_exp_f32_e32 v247, v225
	v_fma_f32 v225, v136, s55, -v201
	v_exp_f32_e32 v166, v166
	v_exp_f32_e32 v168, v167
	v_fma_f32 v167, v140, s55, -v201
	v_exp_f32_e32 v246, v225
	v_exp_f32_e32 v167, v167
	v_fma_f32 v225, v137, s55, -v201
	v_exp_f32_e32 v248, v225
	v_add_f32_e32 v249, v169, v247
	v_add_f32_e32 v225, v166, v168
	v_add_f32_e32 v249, v246, v249
	v_add_f32_e32 v225, v167, v225
	v_fma_f32 v249, 2.0, v249, v245
	v_fma_f32 v225, 2.0, v225, v245
	v_add_f32_e32 v251, v248, v249
	v_add_f32_dpp v253, v248, v248 quad_perm:[1,0,3,2] row_mask:0xf bank_mask:0xf bound_ctrl:1
	v_add_f32_dpp v249, v225, v225 quad_perm:[1,0,3,2] row_mask:0xf bank_mask:0xf bound_ctrl:1
	v_add_f32_dpp v251, v251, v251 quad_perm:[1,0,3,2] row_mask:0xf bank_mask:0xf bound_ctrl:1
	v_mov_b32_dpp v225, v253 quad_perm:[2,3,0,1] row_mask:0xf bank_mask:0xf bound_ctrl:1
	v_mov_b32_dpp v250, v249 quad_perm:[2,3,0,1] row_mask:0xf bank_mask:0xf bound_ctrl:1
	v_mov_b32_dpp v252, v251 quad_perm:[2,3,0,1] row_mask:0xf bank_mask:0xf bound_ctrl:1
	s_and_saveexec_b64 s[0:1], s[8:9]
	s_cbranch_execz .LBB0_573
	v_add_f32_e32 v249, v249, v250
	v_add_f32_e32 v250, v251, v252
	v_add_f32_e32 v225, v253, v225
	s_nop 0
	ds_add_f32 v203, v249 offset:4144
	ds_add_f32 v203, v250 offset:4148
	ds_add_f32 v203, v225 offset:4152

; #define LAS __attribute__((address_space(3)))
; template <int CTRL> __device__ __forceinline__ float dppf(float v) { return __builtin_bit_cast(float, __builtin_amdgcn_update_dpp(0, __builtin_bit_cast(int, v), CTRL, 0xF, 0xF, true)); }
; template <int PASS, bool FULL = false> __device__ __forceinline__ bf16x8 cmp_sm(const f32x4 s0, const f32x4 s1, float& l, float mbi  , LAS float* improw, int kg, int i, int g4, int tq, int j, float mb) {
;     float p[8];
; #pragma unroll
;     for (int r = 0; r < 8; ++r) { const int key = 64 * j + 32 * kg + 8 * g4 + r; const float sv = r < 4 ? s0[r & 3] : s1[r & 3];
;         const float e = __builtin_amdgcn_exp2f(sv * C2_ - (PASS == 1 ? mb : mbi));
;         p[r] = (FULL || 16 * key + 31 <= tq) ? e : 0.f; }
;     if (PASS == 1) { l += ((p[0] + p[1]) + (p[2] + p[3])) + ((p[4] + p[5]) + (p[6] + p[7])); return (bf16x8){0, 0, 0, 0, 0, 0, 0, 0}; }
;     float ia = 2.0f * (p[0] + p[1] + p[2]) + p[3], ib = p[3] + 2.0f * (p[4] + p[5] + p[6]) + p[7], ic = p[7];
;     ia += dppf<0xB1>(ia); ia += dppf<0x4E>(ia); ib += dppf<0xB1>(ib); ib += dppf<0x4E>(ib); ic += dppf<0xB1>(ic); ic += dppf<0x4E>(ic);
;     if ((i & 3) == 0) { LAS float* ip = improw + 16 * j + 8 * kg + 2 * g4;
;         __hip_atomic_fetch_add(ip, ia, __ATOMIC_RELAXED, __HIP_MEMORY_SCOPE_WORKGROUP); __hip_atomic_fetch_add(ip + 1, ib, __ATOMIC_RELAXED, __HIP_MEMORY_SCOPE_WORKGROUP); __hip_atomic_fetch_add(ip + 2, ic, __ATOMIC_RELAXED, __HIP_MEMORY_SCOPE_WORKGROUP); }
;     return pack8(p[0], p[1], p[2], p[3], p[4], p[5], p[6], p[7]);
; template <int PASS> __device__ __forceinline__ void cmp_compute2(LAS const unsigned char* kb, const QF& q0, const QF& q1, f32x4 (&O0)[8], f32x4 (&O1)[8], float& l0, float& l1, float inv0, float inv1, LAS float* imp0, LAS float* imp1, int i, int g4, int tq0, int tq1, int j, float mb, bool full) {
;     ...
;         else { pa0 = cmp_sm<2>(s0, s1, l0, inv0, imp0, 0, i, g4, tq0, j, mb); pb0 = cmp_sm<2>(t0, t1, l0, inv0, imp0, 1, i, g4, tq0, j, mb);
;                pa1 = cmp_sm<2>(u0, u1, l1, inv1, imp1, 0, i, g4, tq1, j, mb); pb1 = cmp_sm<2>(v0, v1, l1, inv1, imp1, 1, i, g4, tq1, j, mb); }
.LBB0_574:
	s_and_b64 vcc, exec, s[0:1]
	s_cbranch_vccz .LBB0_561
	v_exp_f32_e32 v130, v244
	v_add_u32_e32 v150, s10, v219
	v_exp_f32_e32 v131, v243
	v_add_u32_e32 v162, 0xfffffc10, v150
	v_exp_f32_e32 v132, v242
	v_cmp_le_i32_e32 vcc, v162, v1
	v_add_u32_e32 v166, 0xfffffc20, v150
	v_exp_f32_e32 v133, v241
	v_cndmask_b32_e32 v130, 0, v130, vcc
	v_cmp_le_i32_e32 vcc, v166, v1
	v_add_u32_e32 v163, 0xfffffc30, v150
	v_exp_f32_e32 v151, v240
	v_cndmask_b32_e32 v131, 0, v131, vcc
	v_cmp_le_i32_e32 vcc, v163, v1
	v_add_u32_e32 v167, 0xfffffc40, v150
	v_exp_f32_e32 v152, v239
	v_cndmask_b32_e32 v132, 0, v132, vcc
	v_cmp_le_i32_e32 vcc, v167, v1
	v_add_u32_e32 v164, 0xfffffc50, v150
	v_exp_f32_e32 v153, v238
	v_cndmask_b32_e32 v133, 0, v133, vcc
	v_cmp_le_i32_e32 vcc, v164, v1
	v_add_u32_e32 v168, 0xfffffc60, v150
	v_exp_f32_e32 v225, v237
	v_cndmask_b32_e32 v151, 0, v151, vcc
	v_cmp_le_i32_e32 vcc, v168, v1
	v_add_u32_e32 v165, 0xfffffc70, v150
	v_add_u32_e32 v169, 0xfffffc80, v150
	v_cndmask_b32_e32 v152, 0, v152, vcc
	v_cmp_le_i32_e32 vcc, v165, v1
	v_add_f32_e32 v238, v151, v152
	s_nop 0
	v_cndmask_b32_e32 v153, 0, v153, vcc
	v_cmp_le_i32_e32 vcc, v169, v1
	v_add_f32_e32 v238, v153, v238
	v_fma_f32 v238, 2.0, v238, v133
	v_cndmask_b32_e32 v237, 0, v225, vcc
	v_add_f32_e32 v225, v130, v131
	v_add_f32_e32 v225, v132, v225
	v_fma_f32 v225, 2.0, v225, v133
	v_add_f32_e32 v240, v237, v238
	s_nop 0
	v_add_f32_dpp v238, v225, v225 quad_perm:[1,0,3,2] row_mask:0xf bank_mask:0xf bound_ctrl:1
	v_add_f32_dpp v240, v240, v240 quad_perm:[1,0,3,2] row_mask:0xf bank_mask:0xf bound_ctrl:1
	v_add_f32_dpp v225, v237, v237 quad_perm:[1,0,3,2] row_mask:0xf bank_mask:0xf bound_ctrl:1
	v_mov_b32_dpp v239, v238 quad_perm:[2,3,0,1] row_mask:0xf bank_mask:0xf bound_ctrl:1
	v_mov_b32_dpp v241, v240 quad_perm:[2,3,0,1] row_mask:0xf bank_mask:0xf bound_ctrl:1
	v_mov_b32_dpp v242, v225 quad_perm:[2,3,0,1] row_mask:0xf bank_mask:0xf bound_ctrl:1
	s_and_saveexec_b64 s[0:1], s[8:9]
	s_cbranch_execz .LBB0_577
	v_add_f32_e32 v238, v238, v239
	v_add_f32_e32 v225, v225, v242
	v_add_f32_e32 v240, v240, v241
	s_nop 0
	ds_add_f32 v203, v238
	ds_add_f32 v203, v240 offset:4
	ds_add_f32 v203, v225 offset:8
.LBB0_577:
	s_or_b64 exec, exec, s[0:1]
	v_cvt_pk_bf16_f32 v130, v130, v131
	v_cvt_pk_bf16_f32 v131, v132, v133
	v_cvt_pk_bf16_f32 v132, v151, v152
	v_fma_f32 v151, v158, s55, -v199
	v_exp_f32_e32 v151, v151
	v_fma_f32 v152, v159, s55, -v199
	v_cvt_pk_bf16_f32 v133, v153, v237
	v_exp_f32_e32 v152, v152
	v_fma_f32 v153, v160, s55, -v199
	v_add_u32_e32 v158, 0xfffffe10, v150
	v_exp_f32_e32 v153, v153
	v_fma_f32 v160, v161, s55, -v199
	v_cmp_le_i32_e32 vcc, v158, v1
	v_add_u32_e32 v237, 0xfffffe20, v150
	v_exp_f32_e32 v161, v160
	v_cndmask_b32_e32 v151, 0, v151, vcc
	v_cmp_le_i32_e32 vcc, v237, v1
	v_add_u32_e32 v159, 0xfffffe30, v150
	v_add_u32_e32 v160, 0xfffffe40, v150
	v_cndmask_b32_e32 v152, 0, v152, vcc
	v_cmp_le_i32_e32 vcc, v159, v1
	v_fma_f32 v154, v154, s55, -v199
	v_fma_f32 v155, v155, s55, -v199
	v_cndmask_b32_e32 v153, 0, v153, vcc
	v_cmp_le_i32_e32 vcc, v160, v1
	v_exp_f32_e32 v155, v155
	v_fma_f32 v157, v157, s55, -v199
	v_cndmask_b32_e32 v238, 0, v161, vcc
	v_exp_f32_e32 v161, v154
	v_add_u32_e32 v154, 0xfffffe50, v150
	v_cmp_le_i32_e32 vcc, v154, v1
	v_exp_f32_e32 v225, v157
	s_nop 0
	v_cndmask_b32_e32 v239, 0, v161, vcc
	v_add_u32_e32 v161, 0xfffffe60, v150
	v_cmp_le_i32_e32 vcc, v161, v1
	s_nop 1
	v_cndmask_b32_e32 v240, 0, v155, vcc
	v_fma_f32 v155, v156, s55, -v199
	v_exp_f32_e32 v156, v155
	v_add_u32_e32 v155, 0xfffffe70, v150
	v_cmp_le_i32_e32 vcc, v155, v1
	s_nop 1
	v_cndmask_b32_e32 v157, 0, v156, vcc
	v_add_u32_e32 v156, 0xfffffe80, v150
	v_cmp_le_i32_e32 vcc, v156, v1
	v_add_f32_e32 v150, v151, v152
	v_add_f32_e32 v150, v153, v150
	v_cndmask_b32_e32 v241, 0, v225, vcc
	v_add_f32_e32 v225, v239, v240
	v_add_f32_e32 v225, v157, v225
	v_fma_f32 v225, 2.0, v225, v238
	v_fma_f32 v150, 2.0, v150, v238
	v_add_f32_e32 v225, v241, v225
	s_nop 0
	v_add_f32_dpp v150, v150, v150 quad_perm:[1,0,3,2] row_mask:0xf bank_mask:0xf bound_ctrl:1
	v_add_f32_dpp v243, v225, v225 quad_perm:[1,0,3,2] row_mask:0xf bank_mask:0xf bound_ctrl:1
	v_add_f32_dpp v225, v241, v241 quad_perm:[1,0,3,2] row_mask:0xf bank_mask:0xf bound_ctrl:1
	v_mov_b32_dpp v242, v150 quad_perm:[2,3,0,1] row_mask:0xf bank_mask:0xf bound_ctrl:1
	v_mov_b32_dpp v244, v243 quad_perm:[2,3,0,1] row_mask:0xf bank_mask:0xf bound_ctrl:1
	v_mov_b32_dpp v245, v225 quad_perm:[2,3,0,1] row_mask:0xf bank_mask:0xf bound_ctrl:1
	s_and_saveexec_b64 s[0:1], s[8:9]
	s_cbranch_execz .LBB0_579
	v_add_f32_e32 v150, v150, v242
	v_add_f32_e32 v225, v225, v245
	v_add_f32_e32 v243, v243, v244
	s_nop 0
	ds_add_f32 v203, v150 offset:32
	ds_add_f32 v203, v243 offset:36
	ds_add_f32 v203, v225 offset:40
; template <int PASS, bool FULL = false> __device__ __forceinline__ bf16x8 cmp_sm(const f32x4 s0, const f32x4 s1, float& l, float mbi  , LAS float* improw, int kg, int i, int g4, int tq, int j, float mb) {
;     float p[8];
; #pragma unroll
;     for (int r = 0; r < 8; ++r) { const int key = 64 * j + 32 * kg + 8 * g4 + r; const float sv = r < 4 ? s0[r & 3] : s1[r & 3];
;         const float e = __builtin_amdgcn_exp2f(sv * C2_ - (PASS == 1 ? mb : mbi));
;         p[r] = (FULL || 16 * key + 31 <= tq) ? e : 0.f; }
;     if (PASS == 1) { l += ((p[0] + p[1]) + (p[2] + p[3])) + ((p[4] + p[5]) + (p[6] + p[7])); return (bf16x8){0, 0, 0, 0, 0, 0, 0, 0}; }
;     float ia = 2.0f * (p[0] + p[1] + p[2]) + p[3], ib = p[3] + 2.0f * (p[4] + p[5] + p[6]) + p[7], ic = p[7];
;     ia += dppf<0xB1>(ia); ia += dppf<0x4E>(ia); ib += dppf<0xB1>(ib); ib += dppf<0x4E>(ib); ic += dppf<0xB1>(ic); ic += dppf<0x4E>(ic);
;     if ((i & 3) == 0) { LAS float* ip = improw + 16 * j + 8 * kg + 2 * g4;
;         __hip_atomic_fetch_add(ip, ia, __ATOMIC_RELAXED, __HIP_MEMORY_SCOPE_WORKGROUP); __hip_atomic_fetch_add(ip + 1, ib, __ATOMIC_RELAXED, __HIP_MEMORY_SCOPE_WORKGROUP); __hip_atomic_fetch_add(ip + 2, ic, __ATOMIC_RELAXED, __HIP_MEMORY_SCOPE_WORKGROUP); }
;     return pack8(p[0], p[1], p[2], p[3], p[4], p[5], p[6], p[7]);
; }
; template <int PASS> __device__ __forceinline__ void cmp_compute2(LAS const unsigned char* kb, const QF& q0, const QF& q1, f32x4 (&O0)[8], f32x4 (&O1)[8], float& l0, float& l1, float inv0, float inv1, LAS float* imp0, LAS float* imp1, int i, int g4, int tq0, int tq1, int j, float mb, bool full) {
;     ...
;     else { bf16x8 va[8], vc[8], pa0, pb0, pa1, pb1;
;         ta_ldv(vb, 0, i, g4, va); TA_SB;
;         if (full) { pa0 = cmp_sm<2, true>(s0, s1, l0, inv0, imp0, 0, i, g4, tq0, j, mb); pb0 = cmp_sm<2, true>(t0, t1, l0, inv0, imp0, 1, i, g4, tq0, j, mb);
;                     pa1 = cmp_sm<2, true>(u0, u1, l1, inv1, imp1, 0, i, g4, tq1, j, mb); pb1 = cmp_sm<2, true>(v0, v1, l1, inv1, imp1, 1, i, g4, tq1, j, mb); }
;         else { pa0 = cmp_sm<2>(s0, s1, l0, inv0, imp0, 0, i, g4, tq0, j, mb); pb0 = cmp_sm<2>(t0, t1, l0, inv0, imp0, 1, i, g4, tq0, j, mb);
;                pa1 = cmp_sm<2>(u0, u1, l1, inv1, imp1, 0, i, g4, tq1, j, mb); pb1 = cmp_sm<2>(v0, v1, l1, inv1, imp1, 1, i, g4, tq1, j, mb); }
;         TA_SB;
;         ta_ldv(vb, 1, i, g4, vc); TA_SB;
.LBB0_579:
	s_or_b64 exec, exec, s[0:1]
	v_fma_f32 v146, v146, s55, -v201
	v_exp_f32_e32 v146, v146
	v_fma_f32 v147, v147, s55, -v201
	v_exp_f32_e32 v147, v147
	v_fma_f32 v148, v148, s55, -v201
	v_exp_f32_e32 v148, v148
	v_fma_f32 v149, v149, s55, -v201
	v_cmp_le_i32_e32 vcc, v162, v172
	v_exp_f32_e32 v149, v149
	v_fma_f32 v142, v142, s55, -v201
	v_cndmask_b32_e32 v146, 0, v146, vcc
	v_cmp_le_i32_e32 vcc, v166, v172
	v_exp_f32_e32 v142, v142
	v_fma_f32 v143, v143, s55, -v201
	v_cndmask_b32_e32 v147, 0, v147, vcc
	v_cmp_le_i32_e32 vcc, v163, v172
	v_exp_f32_e32 v143, v143
	v_fma_f32 v144, v144, s55, -v201
	v_cndmask_b32_e32 v148, 0, v148, vcc
	v_cmp_le_i32_e32 vcc, v167, v172
	v_exp_f32_e32 v144, v144
	v_fma_f32 v145, v145, s55, -v201
	v_cndmask_b32_e32 v149, 0, v149, vcc
	v_cmp_le_i32_e32 vcc, v164, v172
	v_exp_f32_e32 v145, v145
	v_cvt_pk_bf16_f32 v150, v151, v152
	v_cvt_pk_bf16_f32 v151, v153, v238
	v_cvt_pk_bf16_f32 v152, v239, v240
	v_cvt_pk_bf16_f32 v153, v157, v241
	s_nop 0
	v_cndmask_b32_e32 v142, 0, v142, vcc
	v_cmp_le_i32_e32 vcc, v168, v172
	v_add_f32_e32 v157, v146, v147
	v_add_f32_e32 v157, v148, v157
	v_cndmask_b32_e32 v143, 0, v143, vcc
	v_cmp_le_i32_e32 vcc, v165, v172
	v_add_f32_e32 v162, v142, v143
	v_fma_f32 v157, 2.0, v157, v149
	v_cndmask_b32_e32 v144, 0, v144, vcc
	v_cmp_le_i32_e32 vcc, v169, v172
	v_add_f32_e32 v162, v144, v162
	v_fma_f32 v162, 2.0, v162, v149
	v_cndmask_b32_e32 v145, 0, v145, vcc
	v_add_f32_e32 v163, v145, v162
	v_add_f32_dpp v157, v157, v157 quad_perm:[1,0,3,2] row_mask:0xf bank_mask:0xf bound_ctrl:1
	v_add_f32_dpp v165, v145, v145 quad_perm:[1,0,3,2] row_mask:0xf bank_mask:0xf bound_ctrl:1
	v_add_f32_dpp v163, v163, v163 quad_perm:[1,0,3,2] row_mask:0xf bank_mask:0xf bound_ctrl:1
	v_mov_b32_dpp v162, v157 quad_perm:[2,3,0,1] row_mask:0xf bank_mask:0xf bound_ctrl:1
	v_mov_b32_dpp v166, v165 quad_perm:[2,3,0,1] row_mask:0xf bank_mask:0xf bound_ctrl:1
	v_mov_b32_dpp v164, v163 quad_perm:[2,3,0,1] row_mask:0xf bank_mask:0xf bound_ctrl:1
	s_and_saveexec_b64 s[0:1], s[8:9]
	s_cbranch_execz .LBB0_581
	v_add_f32_e32 v157, v157, v162
	v_add_f32_e32 v165, v165, v166
	v_add_f32_e32 v163, v163, v164
	s_nop 0
	ds_add_f32 v203, v157 offset:4112
	ds_add_f32 v203, v163 offset:4116
	ds_add_f32 v203, v165 offset:4120
.LBB0_581:
	s_or_b64 exec, exec, s[0:1]
	v_fma_f32 v138, v138, s55, -v201
	v_exp_f32_e32 v138, v138
	v_fma_f32 v139, v139, s55, -v201
	v_exp_f32_e32 v139, v139
	v_fma_f32 v140, v140, s55, -v201
	v_exp_f32_e32 v140, v140
	v_fma_f32 v141, v141, s55, -v201
	v_cmp_le_i32_e32 vcc, v158, v172
	v_exp_f32_e32 v141, v141
	v_fma_f32 v134, v134, s55, -v201
	v_cndmask_b32_e32 v138, 0, v138, vcc
	v_cmp_le_i32_e32 vcc, v237, v172
	v_exp_f32_e32 v134, v134
	v_fma_f32 v135, v135, s55, -v201
	v_cndmask_b32_e32 v139, 0, v139, vcc
	v_cmp_le_i32_e32 vcc, v159, v172
	v_exp_f32_e32 v135, v135
	v_fma_f32 v136, v136, s55, -v201
	v_cndmask_b32_e32 v140, 0, v140, vcc
	v_cmp_le_i32_e32 vcc, v160, v172
	v_exp_f32_e32 v136, v136
	v_fma_f32 v137, v137, s55, -v201
	v_cndmask_b32_e32 v141, 0, v141, vcc
	v_cmp_le_i32_e32 vcc, v154, v172
	v_exp_f32_e32 v137, v137
	v_cvt_pk_bf16_f32 v162, v146, v147
	v_cvt_pk_bf16_f32 v163, v148, v149
	v_cvt_pk_bf16_f32 v164, v142, v143
	v_add_f32_e32 v142, v138, v139
	v_cndmask_b32_e32 v134, 0, v134, vcc
	v_cmp_le_i32_e32 vcc, v161, v172
	v_add_f32_e32 v142, v140, v142
	v_cvt_pk_bf16_f32 v165, v144, v145
	v_fma_f32 v142, 2.0, v142, v141
	v_cndmask_b32_e32 v135, 0, v135, vcc
	v_cmp_le_i32_e32 vcc, v155, v172
	v_add_f32_e32 v143, v134, v135
	v_add_f32_dpp v142, v142, v142 quad_perm:[1,0,3,2] row_mask:0xf bank_mask:0xf bound_ctrl:1
	v_cndmask_b32_e32 v136, 0, v136, vcc
	v_cmp_le_i32_e32 vcc, v156, v172
	v_add_f32_e32 v143, v136, v143
	v_fma_f32 v143, 2.0, v143, v141
	v_cndmask_b32_e32 v137, 0, v137, vcc
	v_add_f32_e32 v144, v137, v143
	v_mov_b32_dpp v143, v142 quad_perm:[2,3,0,1] row_mask:0xf bank_mask:0xf bound_ctrl:1
	v_add_f32_dpp v146, v137, v137 quad_perm:[1,0,3,2] row_mask:0xf bank_mask:0xf bound_ctrl:1
	v_add_f32_dpp v144, v144, v144 quad_perm:[1,0,3,2] row_mask:0xf bank_mask:0xf bound_ctrl:1
	s_nop 0
	v_mov_b32_dpp v147, v146 quad_perm:[2,3,0,1] row_mask:0xf bank_mask:0xf bound_ctrl:1
	v_mov_b32_dpp v145, v144 quad_perm:[2,3,0,1] row_mask:0xf bank_mask:0xf bound_ctrl:1
	s_and_saveexec_b64 s[0:1], s[8:9]
	s_cbranch_execz .LBB0_560
	v_add_f32_e32 v142, v142, v143
	v_add_f32_e32 v146, v146, v147
	v_add_f32_e32 v144, v144, v145
	s_nop 0
	ds_add_f32 v203, v142 offset:4144
	ds_add_f32 v203, v144 offset:4148
	ds_add_f32 v203, v146 offset:4152
	s_branch .LBB0_560

;     ...
;         l0 += __shfl_xor(l0, 16); l0 += __shfl_xor(l0, 32); l1 += __shfl_xor(l1, 16); l1 += __shfl_xor(l1, 32);
;         const float* gates = WSP(float, WS_GATES);
;         const float sc0 = (l0 > 0.f ? 1.0f / l0 : 0.f) * gates[tt0 * 24 + hh * 3 + (MODE == MODE_SEL ? 1 : 2)], sc1 = (l1 > 0.f ? 1.0f / l1 : 0.f) * gates[tt1 * 24 + hh * 3 + (MODE == MODE_SEL ? 1 : 2)];
;         float* ma0 = WSP(float, WS_MIXACC) + tt0 * 1024 + hh * 128 + 4 * g4; float* ma1 = WSP(float, WS_MIXACC) + tt1 * 1024 + hh * 128 + 4 * g4;
;         if (DRY) { asm volatile("" :: "v"(sc0), "v"(sc1));
; #pragma unroll
;             for (int dt = 0; dt < 8; ++dt) asm volatile("" :: "v"(O0[dt]), "v"(O1[dt]));
;         } else if (MODE == MODE_SEL) {
;             unsigned char* d0 = WSP(unsigned char, WS_MIX) + tt0 * MIXP + 1024 + hh * 128 + 4 * g4; unsigned char* d1 = WSP(unsigned char, WS_MIX) + tt1 * MIXP + 1024 + hh * 128 + 4 * g4;
; #pragma unroll
;             for (int dt = 0; dt < 8; ++dt) { const f32x4 v0 = (*(const f32x4*)(ma0 + 16 * dt) + O0[dt] * sc0) * MIX_SCALE, v1 = (*(const f32x4*)(ma1 + 16 * dt) + O1[dt] * sc1) * MIX_SCALE;
;                 *(unsigned*)(d0 + 16 * dt) = pk4_fp8(v0[0], v0[1], v0[2], v0[3]); *(unsigned*)(d1 + 16 * dt) = pk4_fp8(v1[0], v1[1], v1[2], v1[3]); }
.LBB0_657:
	s_waitcnt vmcnt(0)
	v_mov_b64_e32 v[72:73], s[36:37]
	v_mul_u32_u24_e32 v74, 3, v219
	v_mad_u64_u32 v[72:73], s[0:1], v220, s70, v[72:73]
	v_lshlrev_b64 v[66:67], 10, v[220:221]
	v_lshlrev_b32_e32 v70, 7, v219
	v_lshlrev_b64 v[68:69], 10, v[222:223]
	v_mad_i32_i24 v73, v221, s70, v73
	v_lshlrev_b32_e32 v74, 2, v74
	v_mov_b32_e32 v75, v201
	v_lshl_add_u64 v[72:73], v[72:73], 0, v[74:75]
	v_lshl_add_u64 v[66:67], v[66:67], 2, s[38:39]
	v_lshlrev_b32_e32 v74, 2, v70
	v_lshl_add_u64 v[68:69], v[68:69], 2, s[38:39]
	v_lshl_add_u64 v[66:67], v[66:67], 0, v[74:75]
	v_mov_b32_e32 v219, v201
	v_lshl_add_u64 v[68:69], v[68:69], 0, v[74:75]
	v_lshl_add_u64 v[66:67], v[66:67], 0, v[218:219]
	global_load_dword v86, v[72:73], off offset:4
	global_load_dword v87, v[72:73], off offset:388
	global_load_dwordx4 v[74:77], v[66:67], off
	v_lshl_add_u64 v[68:69], v[68:69], 0, v[218:219]
	global_load_dwordx4 v[78:81], v[68:69], off
	global_load_dwordx4 v[102:105], v[66:67], off offset:64
	global_load_dwordx4 v[106:109], v[68:69], off offset:64
	global_load_dwordx4 v[110:113], v[66:67], off offset:128
	global_load_dwordx4 v[114:117], v[68:69], off offset:128
	global_load_dwordx4 v[118:121], v[66:67], off offset:192
	global_load_dwordx4 v[122:125], v[68:69], off offset:192
	global_load_dwordx4 v[126:129], v[66:67], off offset:256
	global_load_dwordx4 v[130:133], v[68:69], off offset:256
	global_load_dwordx4 v[170:173], v[66:67], off offset:320
	global_load_dwordx4 v[174:177], v[68:69], off offset:320
	global_load_dwordx4 v[178:181], v[66:67], off offset:384
	global_load_dwordx4 v[182:185], v[68:69], off offset:384
	global_load_dwordx4 v[186:189], v[66:67], off offset:448
	global_load_dwordx4 v[190:193], v[68:69], off offset:448
	v_and_b32_e32 v73, 64, v245
	v_xor_b32_e32 v72, 16, v245
	v_add_u32_e32 v85, 64, v73
	v_cmp_lt_i32_e32 vcc, v72, v85
	v_xor_b32_e32 v84, 32, v245
	v_mov_b64_e32 v[82:83], s[40:41]
	v_cndmask_b32_e32 v72, v245, v72, vcc
	v_lshlrev_b32_e32 v72, 2, v72
	ds_bpermute_b32 v73, v72, v225
	ds_bpermute_b32 v72, v72, v224
	v_cmp_lt_i32_e32 vcc, v84, v85
	v_mad_u64_u32 v[82:83], s[0:1], v220, s71, v[82:83]
	s_nop 0
	v_cndmask_b32_e32 v84, v245, v84, vcc
	v_lshlrev_b32_e32 v84, 2, v84
	s_waitcnt lgkmcnt(0)
	v_pk_add_f32 v[72:73], v[224:225], v[72:73]
	ds_bpermute_b32 v85, v84, v73
	ds_bpermute_b32 v84, v84, v72
	v_mov_b32_e32 v71, v201
	v_mad_i32_i24 v83, v221, s71, v83
	v_lshl_add_u64 v[82:83], v[82:83], 0, v[70:71]
	s_waitcnt lgkmcnt(0)
	v_pk_add_f32 v[70:71], v[72:73], v[84:85]
	s_nop 0
	v_div_scale_f32 v72, s[0:1], v71, v71, 1.0
	v_div_scale_f32 v84, s[0:1], v70, v70, 1.0
	v_rcp_f32_e32 v85, v72
	v_rcp_f32_e32 v88, v84
	v_div_scale_f32 v73, vcc, 1.0, v71, 1.0
	v_fma_f32 v90, -v72, v85, 1.0
	v_fma_f32 v91, -v84, v88, 1.0
	v_fmac_f32_e32 v85, v90, v85
	v_div_scale_f32 v89, s[14:15], 1.0, v70, 1.0
	v_fmac_f32_e32 v88, v91, v88
	v_mul_f32_e32 v90, v73, v85
	v_mul_f32_e32 v91, v89, v88
	v_fma_f32 v92, -v72, v90, v73
	v_fma_f32 v93, -v84, v91, v89
	v_fmac_f32_e32 v90, v92, v85
	v_fmac_f32_e32 v91, v93, v88
	v_fma_f32 v72, -v72, v90, v73
	v_fma_f32 v73, -v84, v91, v89
	v_div_fmas_f32 v72, v72, v85, v90
	s_mov_b64 vcc, s[14:15]
	v_div_fixup_f32 v72, v72, v71, 1.0
	v_div_fmas_f32 v73, v73, v88, v91
	v_cmp_lt_f32_e32 vcc, 0, v71
	v_readlane_b32 s0, v254, 2
	s_add_i32 s73, s73, s0
	v_cndmask_b32_e32 v71, 0, v72, vcc
	v_div_fixup_f32 v72, v73, v70, 1.0
	v_cmp_lt_f32_e32 vcc, 0, v70
	s_cmpk_gt_i32 s73, 0x3ff
	v_readlane_b32 s1, v254, 3
	v_cndmask_b32_e32 v70, 0, v72, vcc
	s_waitcnt vmcnt(17)
	v_mul_f32_e32 v72, v86, v71
	s_waitcnt vmcnt(16)
	v_mul_f32_e32 v70, v87, v70
	s_waitcnt vmcnt(15)
	v_pk_fma_f32 v[62:63], v[62:63], v[72:73], v[74:75] op_sel_hi:[1,0,1]
	v_pk_fma_f32 v[64:65], v[64:65], v[72:73], v[76:77] op_sel_hi:[1,0,1]
	s_waitcnt vmcnt(14)
	v_pk_fma_f32 v[54:55], v[54:55], v[70:71], v[78:79] op_sel_hi:[1,0,1]
	v_pk_mul_f32 v[62:63], v[62:63], s[46:47] op_sel_hi:[1,0]
	v_pk_fma_f32 v[56:57], v[56:57], v[70:71], v[80:81] op_sel_hi:[1,0,1]
	v_pk_mul_f32 v[54:55], v[54:55], s[46:47] op_sel_hi:[1,0]
	v_med3_f32 v62, v62, s72, v246
	v_med3_f32 v63, v63, s72, v246
	v_mov_b32_e32 v71, v201
	v_cvt_pk_fp8_f32 v71, v62, v63
	v_med3_f32 v54, v54, s72, v246
	v_med3_f32 v55, v55, s72, v246
	v_mov_b32_e32 v62, v201
	v_cvt_pk_fp8_f32 v62, v54, v55
	v_pk_mul_f32 v[64:65], v[64:65], s[46:47] op_sel_hi:[1,0]
	v_pk_mul_f32 v[56:57], v[56:57], s[46:47] op_sel_hi:[1,0]
	v_med3_f32 v64, v64, s72, v246
	v_med3_f32 v65, v65, s72, v246
	v_cvt_pk_fp8_f32 v71, v64, v65 op_sel:[0,0,1]
	v_med3_f32 v54, v56, s72, v246
	v_med3_f32 v55, v57, s72, v246
	v_cvt_pk_fp8_f32 v62, v54, v55 op_sel:[0,0,1]
	v_lshl_add_u64 v[54:55], v[82:83], 0, v[210:211]
	v_lshl_add_u64 v[56:57], v[54:55], 0, s[44:45]
	global_store_dword v[54:55], v71, off offset:1024
	global_store_dword v[56:57], v62, off offset:1024
	s_nop 0
	s_nop 0
	s_nop 0
	v_mov_b32_e32 v73, v201
	v_mov_b32_e32 v71, v201
	s_waitcnt vmcnt(15)
	v_pk_fma_f32 v[58:59], v[58:59], v[72:73], v[102:103] op_sel_hi:[1,0,1]
	s_waitcnt vmcnt(14)
	v_pk_fma_f32 v[50:51], v[50:51], v[70:71], v[106:107] op_sel_hi:[1,0,1]
	v_pk_mul_f32 v[58:59], v[58:59], s[46:47] op_sel_hi:[1,0]
	v_pk_mul_f32 v[50:51], v[50:51], s[46:47] op_sel_hi:[1,0]
	v_med3_f32 v58, v58, s72, v246
	v_med3_f32 v59, v59, s72, v246
	v_pk_fma_f32 v[52:53], v[52:53], v[70:71], v[108:109] op_sel_hi:[1,0,1]
	v_med3_f32 v50, v50, s72, v246
	v_med3_f32 v51, v51, s72, v246
	v_cvt_pk_fp8_f32 v71, v58, v59
	v_pk_fma_f32 v[60:61], v[60:61], v[72:73], v[104:105] op_sel_hi:[1,0,1]
	v_cvt_pk_fp8_f32 v73, v50, v51
	v_pk_mul_f32 v[60:61], v[60:61], s[46:47] op_sel_hi:[1,0]
	v_pk_mul_f32 v[52:53], v[52:53], s[46:47] op_sel_hi:[1,0]
	v_med3_f32 v60, v60, s72, v246
	v_med3_f32 v61, v61, s72, v246
	v_med3_f32 v50, v52, s72, v246
	v_med3_f32 v51, v53, s72, v246
	v_cvt_pk_fp8_f32 v71, v60, v61 op_sel:[0,0,1]
	v_cvt_pk_fp8_f32 v73, v50, v51 op_sel:[0,0,1]
	global_store_dword v[54:55], v71, off offset:1040
	global_store_dword v[56:57], v73, off offset:1040
	s_nop 0
	s_nop 0
	v_mov_b32_e32 v62, v201
	v_mov_b32_e32 v63, v201
	s_waitcnt vmcnt(15)
;     ...
;             unsigned char* d0 = WSP(unsigned char, WS_MIX) + tt0 * MIXP + 1024 + hh * 128 + 4 * g4; unsigned char* d1 = WSP(unsigned char, WS_MIX) + tt1 * MIXP + 1024 + hh * 128 + 4 * g4;
; #pragma unroll
;             for (int dt = 0; dt < 8; ++dt) { const f32x4 v0 = (*(const f32x4*)(ma0 + 16 * dt) + O0[dt] * sc0) * MIX_SCALE, v1 = (*(const f32x4*)(ma1 + 16 * dt) + O1[dt] * sc1) * MIX_SCALE;
;                 *(unsigned*)(d0 + 16 * dt) = pk4_fp8(v0[0], v0[1], v0[2], v0[3]); *(unsigned*)(d1 + 16 * dt) = pk4_fp8(v1[0], v1[1], v1[2], v1[3]); }
	v_pk_fma_f32 v[46:47], v[46:47], v[72:73], v[110:111] op_sel_hi:[1,0,1]
	s_waitcnt vmcnt(14)
	v_pk_fma_f32 v[42:43], v[42:43], v[70:71], v[114:115] op_sel_hi:[1,0,1]
	v_pk_mul_f32 v[46:47], v[46:47], s[46:47] op_sel_hi:[1,0]
	v_pk_mul_f32 v[42:43], v[42:43], s[46:47] op_sel_hi:[1,0]
	v_med3_f32 v46, v46, s72, v246
	v_med3_f32 v47, v47, s72, v246
	v_med3_f32 v42, v42, s72, v246
	v_med3_f32 v43, v43, s72, v246
	v_cvt_pk_fp8_f32 v62, v46, v47
	v_pk_fma_f32 v[48:49], v[48:49], v[72:73], v[112:113] op_sel_hi:[1,0,1]
	v_cvt_pk_fp8_f32 v63, v42, v43
	v_pk_fma_f32 v[44:45], v[44:45], v[70:71], v[116:117] op_sel_hi:[1,0,1]
	v_pk_mul_f32 v[48:49], v[48:49], s[46:47] op_sel_hi:[1,0]
	v_pk_mul_f32 v[44:45], v[44:45], s[46:47] op_sel_hi:[1,0]
	v_med3_f32 v48, v48, s72, v246
	v_med3_f32 v49, v49, s72, v246
	v_med3_f32 v42, v44, s72, v246
	v_med3_f32 v43, v45, s72, v246
	v_cvt_pk_fp8_f32 v62, v48, v49 op_sel:[0,0,1]
	v_cvt_pk_fp8_f32 v63, v42, v43 op_sel:[0,0,1]
	global_store_dword v[54:55], v62, off offset:1056
	global_store_dword v[56:57], v63, off offset:1056
	s_nop 0
	s_nop 0
	v_mov_b32_e32 v50, v201
	v_mov_b32_e32 v51, v201
	s_waitcnt vmcnt(15)
	v_pk_fma_f32 v[38:39], v[38:39], v[72:73], v[118:119] op_sel_hi:[1,0,1]
	s_waitcnt vmcnt(14)
	v_pk_fma_f32 v[34:35], v[34:35], v[70:71], v[122:123] op_sel_hi:[1,0,1]
	v_pk_mul_f32 v[38:39], v[38:39], s[46:47] op_sel_hi:[1,0]
	v_pk_mul_f32 v[34:35], v[34:35], s[46:47] op_sel_hi:[1,0]
	v_med3_f32 v38, v38, s72, v246
	v_med3_f32 v39, v39, s72, v246
	v_med3_f32 v34, v34, s72, v246
	v_med3_f32 v35, v35, s72, v246
	v_cvt_pk_fp8_f32 v50, v38, v39
	v_pk_fma_f32 v[40:41], v[40:41], v[72:73], v[120:121] op_sel_hi:[1,0,1]
	v_cvt_pk_fp8_f32 v51, v34, v35
	v_pk_fma_f32 v[36:37], v[36:37], v[70:71], v[124:125] op_sel_hi:[1,0,1]
	v_pk_mul_f32 v[40:41], v[40:41], s[46:47] op_sel_hi:[1,0]
	v_pk_mul_f32 v[36:37], v[36:37], s[46:47] op_sel_hi:[1,0]
	v_med3_f32 v40, v40, s72, v246
	v_med3_f32 v41, v41, s72, v246
	v_med3_f32 v34, v36, s72, v246
	v_med3_f32 v35, v37, s72, v246
	v_cvt_pk_fp8_f32 v50, v40, v41 op_sel:[0,0,1]
	v_cvt_pk_fp8_f32 v51, v34, v35 op_sel:[0,0,1]
	global_store_dword v[54:55], v50, off offset:1072
	global_store_dword v[56:57], v51, off offset:1072
	s_nop 0
	s_nop 0
	v_mov_b32_e32 v42, v201
	v_mov_b32_e32 v43, v201
	s_waitcnt vmcnt(15)
	v_pk_fma_f32 v[30:31], v[30:31], v[72:73], v[126:127] op_sel_hi:[1,0,1]
	s_waitcnt vmcnt(14)
	v_pk_fma_f32 v[26:27], v[26:27], v[70:71], v[130:131] op_sel_hi:[1,0,1]
	v_pk_mul_f32 v[30:31], v[30:31], s[46:47] op_sel_hi:[1,0]
	v_pk_mul_f32 v[26:27], v[26:27], s[46:47] op_sel_hi:[1,0]
	v_med3_f32 v30, v30, s72, v246
	v_med3_f32 v31, v31, s72, v246
	v_med3_f32 v26, v26, s72, v246
	v_med3_f32 v27, v27, s72, v246
	v_cvt_pk_fp8_f32 v42, v30, v31
	v_pk_fma_f32 v[32:33], v[32:33], v[72:73], v[128:129] op_sel_hi:[1,0,1]
	v_cvt_pk_fp8_f32 v43, v26, v27
	v_pk_fma_f32 v[28:29], v[28:29], v[70:71], v[132:133] op_sel_hi:[1,0,1]
	v_pk_mul_f32 v[32:33], v[32:33], s[46:47] op_sel_hi:[1,0]
	v_pk_mul_f32 v[28:29], v[28:29], s[46:47] op_sel_hi:[1,0]
	v_med3_f32 v32, v32, s72, v246
	v_med3_f32 v33, v33, s72, v246
	v_med3_f32 v26, v28, s72, v246
	v_med3_f32 v27, v29, s72, v246
	v_cvt_pk_fp8_f32 v42, v32, v33 op_sel:[0,0,1]
	v_cvt_pk_fp8_f32 v43, v26, v27 op_sel:[0,0,1]
	global_store_dword v[54:55], v42, off offset:1088
	global_store_dword v[56:57], v43, off offset:1088
	s_nop 0
	s_nop 0
	v_mov_b32_e32 v34, v201
	v_mov_b32_e32 v35, v201
	s_waitcnt vmcnt(15)
	v_pk_fma_f32 v[22:23], v[22:23], v[72:73], v[170:171] op_sel_hi:[1,0,1]
	s_waitcnt vmcnt(14)
	v_pk_fma_f32 v[18:19], v[18:19], v[70:71], v[174:175] op_sel_hi:[1,0,1]
	v_pk_mul_f32 v[22:23], v[22:23], s[46:47] op_sel_hi:[1,0]
	v_pk_mul_f32 v[18:19], v[18:19], s[46:47] op_sel_hi:[1,0]
	v_med3_f32 v22, v22, s72, v246
	v_med3_f32 v23, v23, s72, v246
	v_med3_f32 v18, v18, s72, v246
	v_med3_f32 v19, v19, s72, v246
	v_cvt_pk_fp8_f32 v34, v22, v23
	v_pk_fma_f32 v[24:25], v[24:25], v[72:73], v[172:173] op_sel_hi:[1,0,1]
	v_cvt_pk_fp8_f32 v35, v18, v19
	v_pk_fma_f32 v[20:21], v[20:21], v[70:71], v[176:177] op_sel_hi:[1,0,1]
	v_pk_mul_f32 v[24:25], v[24:25], s[46:47] op_sel_hi:[1,0]
	v_pk_mul_f32 v[20:21], v[20:21], s[46:47] op_sel_hi:[1,0]
	v_med3_f32 v24, v24, s72, v246
	v_med3_f32 v25, v25, s72, v246
	v_med3_f32 v18, v20, s72, v246
	v_med3_f32 v19, v21, s72, v246
	v_cvt_pk_fp8_f32 v34, v24, v25 op_sel:[0,0,1]
	v_cvt_pk_fp8_f32 v35, v18, v19 op_sel:[0,0,1]
	global_store_dword v[54:55], v34, off offset:1104
	global_store_dword v[56:57], v35, off offset:1104
	s_nop 0
	s_nop 0
	v_mov_b32_e32 v26, v201
	v_mov_b32_e32 v27, v201
	s_waitcnt vmcnt(15)
	v_pk_fma_f32 v[14:15], v[14:15], v[72:73], v[178:179] op_sel_hi:[1,0,1]
	s_waitcnt vmcnt(14)
	v_pk_fma_f32 v[10:11], v[10:11], v[70:71], v[182:183] op_sel_hi:[1,0,1]
	v_pk_mul_f32 v[14:15], v[14:15], s[46:47] op_sel_hi:[1,0]
	v_pk_mul_f32 v[10:11], v[10:11], s[46:47] op_sel_hi:[1,0]
	v_med3_f32 v14, v14, s72, v246
	v_med3_f32 v15, v15, s72, v246
	v_med3_f32 v10, v10, s72, v246
	v_med3_f32 v11, v11, s72, v246
	v_cvt_pk_fp8_f32 v26, v14, v15
	v_pk_fma_f32 v[16:17], v[16:17], v[72:73], v[180:181] op_sel_hi:[1,0,1]
	v_cvt_pk_fp8_f32 v27, v10, v11
	v_pk_fma_f32 v[12:13], v[12:13], v[70:71], v[184:185] op_sel_hi:[1,0,1]
	v_pk_mul_f32 v[16:17], v[16:17], s[46:47] op_sel_hi:[1,0]
	v_pk_mul_f32 v[12:13], v[12:13], s[46:47] op_sel_hi:[1,0]
	v_med3_f32 v16, v16, s72, v246
	v_med3_f32 v17, v17, s72, v246
	v_med3_f32 v10, v12, s72, v246
	v_med3_f32 v11, v13, s72, v246
	v_cvt_pk_fp8_f32 v26, v16, v17 op_sel:[0,0,1]
	v_cvt_pk_fp8_f32 v27, v10, v11 op_sel:[0,0,1]
	global_store_dword v[54:55], v26, off offset:1120
	global_store_dword v[56:57], v27, off offset:1120
	s_nop 0
	s_nop 0
	v_mov_b32_e32 v18, v201
	v_mov_b32_e32 v19, v201
	s_waitcnt vmcnt(15)
	v_pk_fma_f32 v[6:7], v[6:7], v[72:73], v[186:187] op_sel_hi:[1,0,1]
	s_waitcnt vmcnt(14)
	v_pk_fma_f32 v[2:3], v[2:3], v[70:71], v[190:191] op_sel_hi:[1,0,1]
	v_pk_mul_f32 v[6:7], v[6:7], s[46:47] op_sel_hi:[1,0]
	v_pk_mul_f32 v[2:3], v[2:3], s[46:47] op_sel_hi:[1,0]
	v_med3_f32 v6, v6, s72, v246
	v_med3_f32 v7, v7, s72, v246
	v_med3_f32 v2, v2, s72, v246
	v_med3_f32 v3, v3, s72, v246
	v_cvt_pk_fp8_f32 v18, v6, v7
	v_pk_fma_f32 v[8:9], v[8:9], v[72:73], v[188:189] op_sel_hi:[1,0,1]
	v_cvt_pk_fp8_f32 v19, v2, v3
	v_pk_fma_f32 v[4:5], v[4:5], v[70:71], v[192:193] op_sel_hi:[1,0,1]
	v_pk_mul_f32 v[8:9], v[8:9], s[46:47] op_sel_hi:[1,0]
	v_pk_mul_f32 v[4:5], v[4:5], s[46:47] op_sel_hi:[1,0]
	v_med3_f32 v8, v8, s72, v246
	v_med3_f32 v9, v9, s72, v246
	v_med3_f32 v2, v4, s72, v246
	v_med3_f32 v3, v5, s72, v246
	v_cvt_pk_fp8_f32 v18, v8, v9 op_sel:[0,0,1]
	v_cvt_pk_fp8_f32 v19, v2, v3 op_sel:[0,0,1]
	global_store_dword v[54:55], v18, off offset:1136
	global_store_dword v[56:57], v19, off offset:1136
	s_barrier
	s_cbranch_scc1 .LBB0_750
